# P2 MMA4: the four per-register lgkm wait pairs merged and the four formerly inserted streamer multiplies placed in the freed slots (no net inserted issue slots for the scale)
# speedup vs baseline: 1.0141x; 1.0137x over previous
.Lp2_top:
	ds_read_b128 v[158:161], v217
	ds_read_b128 v[162:165], v218
	ds_read_b128 v[166:169], v219
	ds_read_b128 v[170:173], v220
	ds_read_b128 v[148:151], v221
	ds_read_b128 v[144:147], v222
	ds_read_b128 v[140:143], v223
	ds_read_b128 v[136:139], v224
	ds_read_b128 v[174:177], v233
	ds_read_b128 v[178:181], v233 offset:1024
	ds_read_b128 v[182:185], v233 offset:2048
	ds_read_b128 v[186:189], v233 offset:3072
	ds_read_b128 v[190:193], v233 offset:4096
	ds_read_b128 v[194:197], v233 offset:5120
	ds_read_b128 v[234:237], v233 offset:6144
	ds_read_b128 v[238:241], v233 offset:7168
	s_add_i32 s4, s60, s61
	s_mov_b32 s46, s94
	s_add_i32 s94, s94, 1
	s_add_i32 s5, s4, 0x200
	s_add_i32 s16, s33, s61
	s_cmpk_eq_i32 s61, 0x1e00
	s_cselect_b32 s47, s90, s5
	s_cselect_b32 s97, s91, s16
	s_add_i32 s96, s47, 0x80
	s_mov_b32 m0, s82
	s_add_i32 s5, s4, 0x100180
	buffer_load_dwordx4 v214, s[8:11], s5 offen lds
	s_add_i32 s4, s4, 0x180180
	s_mov_b32 m0, s85
	s_add_i32 vcc_lo, s97, 0x80
	buffer_load_dwordx4 v214, s[8:11], s4 offen lds
	s_lshr_b32 s4, s94, 2
	s_mul_i32 s5, s4, s34
	s_add_i32 s16, s5, s2
	s_cmp_lt_i32 s4, s3
	s_cselect_b64 s[4:5], -1, 0
	s_and_b64 s[44:45], s[4:5], exec
	s_cselect_b32 s16, s16, 0
	s_bfe_u32 s17, s94, 0x10001
	s_or_b32 s17, s17, s83
	s_bfe_u32 s67, s16, 0x50007
	s_bfe_u32 s36, s16, 0x50002
	s_and_b32 s95, s16, 3
	s_cmpk_gt_i32 s16, 0xfff
	s_cselect_b64 s[44:45], -1, 0
	v_lshl_or_b32 v156, s17, 3, v216
	s_and_b64 s[16:17], s[44:45], exec
	s_cselect_b32 s16, s25, s21
	s_cselect_b32 s17, s24, s20
	s_lshl_b32 vcc_hi, s67, 23
	s_add_u32 s17, s17, vcc_hi
	s_addc_u32 s16, s16, 0
	s_lshl_b32 vcc_hi, s36, 18
	s_add_u32 s17, s17, vcc_hi
	s_addc_u32 vcc_hi, s16, 0
	s_lshl_b32 s16, s95, 9
	s_add_u32 s16, s17, s16
	v_and_or_b32 v204, s66, 2, v200
	s_addc_u32 s17, vcc_hi, 0
	v_lshlrev_b64 v[128:129], 11, v[204:205]
	v_lshl_add_u64 v[128:129], s[16:17], 0, v[128:129]
	v_lshlrev_b32_e32 v204, 4, v156
	v_lshl_add_u64 v[132:133], v[128:129], 0, v[204:205]
	global_load_dwordx4 v[128:131], v[132:133], off nt
	s_nop 0
	global_load_dwordx4 v[132:135], v[132:133], off offset:2048 nt
	s_waitcnt vmcnt(10)
	s_waitcnt lgkmcnt(8)
	s_barrier
	s_setprio 1
	s_waitcnt lgkmcnt(7)
	v_mfma_f32_16x16x32_bf16 v[124:127], v[158:161], v[174:177], v[124:127]
	s_waitcnt lgkmcnt(6)
	v_mfma_f32_16x16x32_bf16 v[124:127], v[162:165], v[178:181], v[124:127]
	v_mfma_f32_16x16x32_bf16 v[120:123], v[166:169], v[174:177], v[120:123]
	s_nop 0
	v_mfma_f32_16x16x32_bf16 v[120:123], v[170:173], v[178:181], v[120:123]
	s_waitcnt lgkmcnt(5)
	v_mfma_f32_16x16x32_bf16 v[116:119], v[158:161], v[182:185], v[116:119]
	s_waitcnt lgkmcnt(4)
	v_mfma_f32_16x16x32_bf16 v[116:119], v[162:165], v[186:189], v[116:119]
	v_mfma_f32_16x16x32_bf16 v[112:115], v[166:169], v[182:185], v[112:115]
	s_nop 0
	v_mfma_f32_16x16x32_bf16 v[112:115], v[170:173], v[186:189], v[112:115]
	s_waitcnt lgkmcnt(3)
	v_mfma_f32_16x16x32_bf16 v[108:111], v[158:161], v[190:193], v[108:111]
	s_waitcnt lgkmcnt(2)
	v_mfma_f32_16x16x32_bf16 v[108:111], v[162:165], v[194:197], v[108:111]
	v_mfma_f32_16x16x32_bf16 v[104:107], v[166:169], v[190:193], v[104:107]
	s_nop 0
	v_mfma_f32_16x16x32_bf16 v[104:107], v[170:173], v[194:197], v[104:107]
	s_waitcnt lgkmcnt(1)
	v_mfma_f32_16x16x32_bf16 v[100:103], v[158:161], v[234:237], v[100:103]
	s_waitcnt lgkmcnt(0)
	v_mfma_f32_16x16x32_bf16 v[100:103], v[162:165], v[238:241], v[100:103]
	v_mfma_f32_16x16x32_bf16 v[96:99], v[166:169], v[234:237], v[96:99]
	s_nop 0
	v_mfma_f32_16x16x32_bf16 v[96:99], v[170:173], v[238:241], v[96:99]
	s_setprio 0
	s_setprio 1
	v_mfma_f32_16x16x32_bf16 v[92:95], v[148:151], v[174:177], v[92:95]
	s_nop 0
	v_mfma_f32_16x16x32_bf16 v[92:95], v[144:147], v[178:181], v[92:95]
	v_mfma_f32_16x16x32_bf16 v[88:91], v[140:143], v[174:177], v[88:91]
	s_nop 0
	v_mfma_f32_16x16x32_bf16 v[88:91], v[136:139], v[178:181], v[88:91]
	v_mfma_f32_16x16x32_bf16 v[84:87], v[148:151], v[182:185], v[84:87]
	s_nop 0
	v_mfma_f32_16x16x32_bf16 v[84:87], v[144:147], v[186:189], v[84:87]
	v_mfma_f32_16x16x32_bf16 v[80:83], v[140:143], v[182:185], v[80:83]
	s_nop 0
	v_mfma_f32_16x16x32_bf16 v[80:83], v[136:139], v[186:189], v[80:83]
	v_mfma_f32_16x16x32_bf16 v[76:79], v[148:151], v[190:193], v[76:79]
	s_nop 0
	v_mfma_f32_16x16x32_bf16 v[76:79], v[144:147], v[194:197], v[76:79]
	v_mfma_f32_16x16x32_bf16 v[72:75], v[140:143], v[190:193], v[72:75]
	s_nop 0
	v_mfma_f32_16x16x32_bf16 v[72:75], v[136:139], v[194:197], v[72:75]
	v_mfma_f32_16x16x32_bf16 v[68:71], v[148:151], v[234:237], v[68:71]
	s_nop 0
	v_mfma_f32_16x16x32_bf16 v[68:71], v[144:147], v[238:241], v[68:71]
	v_mfma_f32_16x16x32_bf16 v[64:67], v[140:143], v[234:237], v[64:67]
	s_nop 0
	v_mfma_f32_16x16x32_bf16 v[64:67], v[136:139], v[238:241], v[64:67]
	s_setprio 0
	s_barrier
	ds_read_b128 v[174:177], v233 offset:16384
	ds_read_b128 v[178:181], v233 offset:17408
	ds_read_b128 v[182:185], v233 offset:18432
	ds_read_b128 v[186:189], v233 offset:19456
	ds_read_b128 v[190:193], v233 offset:20480
	ds_read_b128 v[194:197], v233 offset:21504
	ds_read_b128 v[234:237], v233 offset:22528
	ds_read_b128 v[238:241], v233 offset:23552
	s_mov_b32 m0, s65
	s_add_i32 s16, s97, 0x100000
	buffer_load_dwordx4 v215, s[12:15], s97 offen lds
	s_mov_b32 m0, s68
	s_nop 0
	buffer_load_dwordx4 v215, s[12:15], s16 offen lds
	s_add_i32 s16, s97, 0x10000
	s_mov_b32 m0, s69
	s_nop 0
	buffer_load_dwordx4 v215, s[12:15], s16 offen lds
	s_add_i32 s16, s97, 0x110000
	s_mov_b32 m0, s70
	s_nop 0
	buffer_load_dwordx4 v215, s[12:15], s16 offen lds
	s_mov_b32 m0, s64
	s_add_i32 s16, s47, 0x80000
	buffer_load_dwordx4 v214, s[8:11], s47 offen lds
	s_mov_b32 m0, s71
	s_nop 0
	buffer_load_dwordx4 v214, s[8:11], s16 offen lds
	s_waitcnt vmcnt(10)
	s_waitcnt lgkmcnt(6)
	s_barrier
	s_setprio 1
	s_waitcnt lgkmcnt(7)
	v_mfma_f32_16x16x32_bf16 v[60:63], v[158:161], v[174:177], v[60:63]
	s_waitcnt lgkmcnt(6)
	v_mfma_f32_16x16x32_bf16 v[60:63], v[162:165], v[178:181], v[60:63]
	v_mfma_f32_16x16x32_bf16 v[56:59], v[166:169], v[174:177], v[56:59]
	s_nop 0
	v_mfma_f32_16x16x32_bf16 v[56:59], v[170:173], v[178:181], v[56:59]
	s_waitcnt lgkmcnt(5)
	v_mfma_f32_16x16x32_bf16 v[52:55], v[158:161], v[182:185], v[52:55]
	s_waitcnt lgkmcnt(4)
	v_mfma_f32_16x16x32_bf16 v[52:55], v[162:165], v[186:189], v[52:55]
	v_mfma_f32_16x16x32_bf16 v[48:51], v[166:169], v[182:185], v[48:51]
	s_nop 0
	v_mfma_f32_16x16x32_bf16 v[48:51], v[170:173], v[186:189], v[48:51]
	s_waitcnt lgkmcnt(3)
	v_mfma_f32_16x16x32_bf16 v[44:47], v[158:161], v[190:193], v[44:47]
	s_waitcnt lgkmcnt(2)
	v_mfma_f32_16x16x32_bf16 v[44:47], v[162:165], v[194:197], v[44:47]
	v_mfma_f32_16x16x32_bf16 v[40:43], v[166:169], v[190:193], v[40:43]
	s_nop 0
	v_mfma_f32_16x16x32_bf16 v[40:43], v[170:173], v[194:197], v[40:43]
	s_waitcnt lgkmcnt(1)
	v_mfma_f32_16x16x32_bf16 v[36:39], v[158:161], v[234:237], v[36:39]
	s_waitcnt lgkmcnt(0)
	v_mfma_f32_16x16x32_bf16 v[36:39], v[162:165], v[238:241], v[36:39]
	v_mfma_f32_16x16x32_bf16 v[32:35], v[166:169], v[234:237], v[32:35]
	s_nop 0
	v_mfma_f32_16x16x32_bf16 v[32:35], v[170:173], v[238:241], v[32:35]
	s_setprio 0
	s_setprio 1
	v_mfma_f32_16x16x32_bf16 v[28:31], v[148:151], v[174:177], v[28:31]
	s_nop 0
	v_mfma_f32_16x16x32_bf16 v[28:31], v[144:147], v[178:181], v[28:31]
	v_mfma_f32_16x16x32_bf16 v[24:27], v[140:143], v[174:177], v[24:27]
	s_nop 0
	v_mfma_f32_16x16x32_bf16 v[24:27], v[136:139], v[178:181], v[24:27]
	v_mfma_f32_16x16x32_bf16 v[20:23], v[148:151], v[182:185], v[20:23]
	s_nop 0
	v_mfma_f32_16x16x32_bf16 v[20:23], v[144:147], v[186:189], v[20:23]
	v_mfma_f32_16x16x32_bf16 v[16:19], v[140:143], v[182:185], v[16:19]
	s_nop 0
	v_mfma_f32_16x16x32_bf16 v[16:19], v[136:139], v[186:189], v[16:19]
	v_mfma_f32_16x16x32_bf16 v[12:15], v[148:151], v[190:193], v[12:15]
	s_nop 0
	v_mfma_f32_16x16x32_bf16 v[12:15], v[144:147], v[194:197], v[12:15]
	v_mfma_f32_16x16x32_bf16 v[8:11], v[140:143], v[190:193], v[8:11]
	s_nop 0
	v_mfma_f32_16x16x32_bf16 v[8:11], v[136:139], v[194:197], v[8:11]
	v_mfma_f32_16x16x32_bf16 v[4:7], v[148:151], v[234:237], v[4:7]
	s_nop 0
	v_mfma_f32_16x16x32_bf16 v[4:7], v[144:147], v[238:241], v[4:7]
	v_mfma_f32_16x16x32_bf16 v[0:3], v[140:143], v[234:237], v[0:3]
	s_nop 0
	v_mfma_f32_16x16x32_bf16 v[0:3], v[136:139], v[238:241], v[0:3]
	s_setprio 0
	s_barrier
	ds_read_b128 v[136:139], v225
	ds_read_b128 v[140:143], v226
	ds_read_b128 v[144:147], v227
	ds_read_b128 v[148:151], v228
	ds_read_b128 v[158:161], v229
	ds_read_b128 v[162:165], v230
	ds_read_b128 v[166:169], v231
	ds_read_b128 v[170:173], v232
	ds_read_b128 v[174:177], v233 offset:32768
	ds_read_b128 v[178:181], v233 offset:33792
	ds_read_b128 v[182:185], v233 offset:34816
	ds_read_b128 v[186:189], v233 offset:35840
	ds_read_b128 v[190:193], v233 offset:36864
	ds_read_b128 v[194:197], v233 offset:37888
	ds_read_b128 v[234:237], v233 offset:38912
	ds_read_b128 v[238:241], v233 offset:39936
	s_mov_b32 m0, s72
	s_add_i32 s16, s47, 0x100000
	buffer_load_dwordx4 v214, s[8:11], s16 offen lds
	s_add_i32 s16, s47, 0x180000
	s_mov_b32 m0, s73
	s_nop 0
	buffer_load_dwordx4 v214, s[8:11], s16 offen lds
	s_waitcnt vmcnt(10)
	s_waitcnt lgkmcnt(8)
	s_barrier
	s_setprio 1
	s_waitcnt lgkmcnt(7)
	v_mfma_f32_16x16x32_bf16 v[124:127], v[136:139], v[174:177], v[124:127]
	s_waitcnt lgkmcnt(6)
	v_mfma_f32_16x16x32_bf16 v[124:127], v[140:143], v[178:181], v[124:127]
	v_mfma_f32_16x16x32_bf16 v[120:123], v[144:147], v[174:177], v[120:123]
	s_nop 0
	v_mfma_f32_16x16x32_bf16 v[120:123], v[148:151], v[178:181], v[120:123]
	s_waitcnt lgkmcnt(5)
	v_mfma_f32_16x16x32_bf16 v[116:119], v[136:139], v[182:185], v[116:119]
	s_waitcnt lgkmcnt(4)
	v_mfma_f32_16x16x32_bf16 v[116:119], v[140:143], v[186:189], v[116:119]
	v_mfma_f32_16x16x32_bf16 v[112:115], v[144:147], v[182:185], v[112:115]
	s_nop 0
	v_mfma_f32_16x16x32_bf16 v[112:115], v[148:151], v[186:189], v[112:115]
	s_waitcnt lgkmcnt(3)
	v_mfma_f32_16x16x32_bf16 v[108:111], v[136:139], v[190:193], v[108:111]
	s_waitcnt lgkmcnt(2)
	v_mfma_f32_16x16x32_bf16 v[108:111], v[140:143], v[194:197], v[108:111]
	v_mfma_f32_16x16x32_bf16 v[104:107], v[144:147], v[190:193], v[104:107]
	s_nop 0
	v_mfma_f32_16x16x32_bf16 v[104:107], v[148:151], v[194:197], v[104:107]
	s_waitcnt lgkmcnt(1)
	v_mfma_f32_16x16x32_bf16 v[100:103], v[136:139], v[234:237], v[100:103]
	s_waitcnt lgkmcnt(0)
	v_mfma_f32_16x16x32_bf16 v[100:103], v[140:143], v[238:241], v[100:103]
	v_mfma_f32_16x16x32_bf16 v[96:99], v[144:147], v[234:237], v[96:99]
	s_nop 0
	v_mfma_f32_16x16x32_bf16 v[96:99], v[148:151], v[238:241], v[96:99]
	s_setprio 0
	s_setprio 1
	v_mfma_f32_16x16x32_bf16 v[92:95], v[158:161], v[174:177], v[92:95]
	s_nop 0
	v_mfma_f32_16x16x32_bf16 v[92:95], v[162:165], v[178:181], v[92:95]
	v_mfma_f32_16x16x32_bf16 v[88:91], v[166:169], v[174:177], v[88:91]
	s_nop 0
	v_mfma_f32_16x16x32_bf16 v[88:91], v[170:173], v[178:181], v[88:91]
	v_mfma_f32_16x16x32_bf16 v[84:87], v[158:161], v[182:185], v[84:87]
	s_nop 0
	v_mfma_f32_16x16x32_bf16 v[84:87], v[162:165], v[186:189], v[84:87]
	v_mfma_f32_16x16x32_bf16 v[80:83], v[166:169], v[182:185], v[80:83]
	s_nop 0
	v_mfma_f32_16x16x32_bf16 v[80:83], v[170:173], v[186:189], v[80:83]
	v_mfma_f32_16x16x32_bf16 v[76:79], v[158:161], v[190:193], v[76:79]
	s_nop 0
	v_mfma_f32_16x16x32_bf16 v[76:79], v[162:165], v[194:197], v[76:79]
	v_mfma_f32_16x16x32_bf16 v[72:75], v[166:169], v[190:193], v[72:75]
	s_nop 0
	v_mfma_f32_16x16x32_bf16 v[72:75], v[170:173], v[194:197], v[72:75]
	v_mfma_f32_16x16x32_bf16 v[68:71], v[158:161], v[234:237], v[68:71]
	s_nop 0
	v_mfma_f32_16x16x32_bf16 v[68:71], v[162:165], v[238:241], v[68:71]
	v_mfma_f32_16x16x32_bf16 v[64:67], v[166:169], v[234:237], v[64:67]
	s_nop 0
	v_mfma_f32_16x16x32_bf16 v[64:67], v[170:173], v[238:241], v[64:67]
	s_setprio 0
	s_barrier
	ds_read_b128 v[174:177], v233 offset:49152
	ds_read_b128 v[178:181], v233 offset:50176
	ds_read_b128 v[182:185], v233 offset:51200
	ds_read_b128 v[186:189], v233 offset:52224
	ds_read_b128 v[190:193], v233 offset:53248
	ds_read_b128 v[194:197], v233 offset:54272
	ds_read_b128 v[234:237], v233 offset:55296
	ds_read_b128 v[238:241], v233 offset:56320
	s_mov_b32 m0, s76
	s_add_i32 s16, s97, 0x100080
	buffer_load_dwordx4 v215, s[12:15], vcc_lo offen lds
	s_mov_b32 m0, s77
	s_add_i32 s47, s47, 0x80080
	buffer_load_dwordx4 v215, s[12:15], s16 offen lds
	s_add_i32 s16, s97, 0x10080
	s_mov_b32 m0, s80
	s_add_i32 s97, s97, 0x110080
	buffer_load_dwordx4 v215, s[12:15], s16 offen lds
	s_mov_b32 m0, s81
	s_nop 0
	buffer_load_dwordx4 v215, s[12:15], s97 offen lds
	s_mov_b32 m0, s78
	s_nop 0
	buffer_load_dwordx4 v214, s[8:11], s96 offen lds
	s_mov_b32 m0, s79
	s_nop 0
	buffer_load_dwordx4 v214, s[8:11], s47 offen lds
	s_bitcmp0_b32 s46, 0
	s_mov_b32 s98, 0xffff
	s_cselect_b32 s98, 0xffff0000, s98
	s_waitcnt vmcnt(8)
	s_waitcnt lgkmcnt(6)
	s_barrier
	s_setprio 1
	s_waitcnt lgkmcnt(6)
	v_mfma_f32_16x16x32_bf16 v[60:63], v[136:139], v[174:177], v[60:63]
	v_mul_f32_e32 v130, 0x42800000, v130
	v_mfma_f32_16x16x32_bf16 v[60:63], v[140:143], v[178:181], v[60:63]
	v_mfma_f32_16x16x32_bf16 v[56:59], v[144:147], v[174:177], v[56:59]
	v_mul_f32_e32 v128, 0x42800000, v128
	v_mfma_f32_16x16x32_bf16 v[56:59], v[148:151], v[178:181], v[56:59]
	s_waitcnt lgkmcnt(4)
	v_mfma_f32_16x16x32_bf16 v[52:55], v[136:139], v[182:185], v[52:55]
	v_mul_f32_e32 v134, 0x42800000, v134
	v_mfma_f32_16x16x32_bf16 v[52:55], v[140:143], v[186:189], v[52:55]
	v_mfma_f32_16x16x32_bf16 v[48:51], v[144:147], v[182:185], v[48:51]
	v_mul_f32_e32 v132, 0x42800000, v132
	v_mfma_f32_16x16x32_bf16 v[48:51], v[148:151], v[186:189], v[48:51]
	s_waitcnt lgkmcnt(2)
	v_mfma_f32_16x16x32_bf16 v[44:47], v[136:139], v[190:193], v[44:47]
	v_mul_f32_e32 v131, 0x42800000, v131
	v_mfma_f32_16x16x32_bf16 v[44:47], v[140:143], v[194:197], v[44:47]
	v_mfma_f32_16x16x32_bf16 v[40:43], v[144:147], v[190:193], v[40:43]
	v_mul_f32_e32 v129, 0x42800000, v129
	v_mfma_f32_16x16x32_bf16 v[40:43], v[148:151], v[194:197], v[40:43]
	s_waitcnt lgkmcnt(0)
	v_mfma_f32_16x16x32_bf16 v[36:39], v[136:139], v[234:237], v[36:39]
	v_mul_f32_e32 v135, 0x42800000, v135
	v_mfma_f32_16x16x32_bf16 v[36:39], v[140:143], v[238:241], v[36:39]
	v_mfma_f32_16x16x32_bf16 v[32:35], v[144:147], v[234:237], v[32:35]
	v_mul_f32_e32 v133, 0x42800000, v133
	v_mfma_f32_16x16x32_bf16 v[32:35], v[148:151], v[238:241], v[32:35]
	s_setprio 0
	s_setprio 1
	v_mfma_f32_16x16x32_bf16 v[28:31], v[158:161], v[174:177], v[28:31]
	v_cvt_pk_fp8_f32 v204, v128, v132
	v_mfma_f32_16x16x32_bf16 v[28:31], v[162:165], v[178:181], v[28:31]
	v_mfma_f32_16x16x32_bf16 v[24:27], v[166:169], v[174:177], v[24:27]
	v_cvt_pk_fp8_f32 v204, v128, v132 op_sel:[0,0,1]
	v_mfma_f32_16x16x32_bf16 v[24:27], v[170:173], v[178:181], v[24:27]
	v_mfma_f32_16x16x32_bf16 v[20:23], v[158:161], v[182:185], v[20:23]
	v_cvt_pk_fp8_f32 v250, v129, v133
	v_mfma_f32_16x16x32_bf16 v[20:23], v[162:165], v[186:189], v[20:23]
	v_mfma_f32_16x16x32_bf16 v[16:19], v[166:169], v[182:185], v[16:19]
	v_cvt_pk_fp8_f32 v250, v129, v133 op_sel:[0,0,1]
	v_mfma_f32_16x16x32_bf16 v[16:19], v[170:173], v[186:189], v[16:19]
	v_mfma_f32_16x16x32_bf16 v[12:15], v[158:161], v[190:193], v[12:15]
	v_cvt_pk_fp8_f32 v251, v130, v134
	v_mfma_f32_16x16x32_bf16 v[12:15], v[162:165], v[194:197], v[12:15]
	v_bfi_b32 v152, s98, v204, v152
	v_mfma_f32_16x16x32_bf16 v[8:11], v[166:169], v[190:193], v[8:11]
	v_cvt_pk_fp8_f32 v251, v130, v134 op_sel:[0,0,1]
	v_mfma_f32_16x16x32_bf16 v[8:11], v[170:173], v[194:197], v[8:11]
	v_bfi_b32 v153, s98, v250, v153
	v_mfma_f32_16x16x32_bf16 v[4:7], v[158:161], v[234:237], v[4:7]
	v_cvt_pk_fp8_f32 v252, v131, v135
	v_mfma_f32_16x16x32_bf16 v[4:7], v[162:165], v[238:241], v[4:7]
	v_bfi_b32 v154, s98, v251, v154
	v_mfma_f32_16x16x32_bf16 v[0:3], v[166:169], v[234:237], v[0:3]
	v_cvt_pk_fp8_f32 v252, v131, v135 op_sel:[0,0,1]
	v_mfma_f32_16x16x32_bf16 v[0:3], v[170:173], v[238:241], v[0:3]
	v_bfi_b32 v155, s98, v252, v155
	s_setprio 0
	s_barrier
	s_bitcmp0_b32 s46, 0
	s_mov_b64 s[46:47], -1
	s_cbranch_scc0 .LBB0_345
	s_andn2_b64 vcc, exec, s[4:5]
	s_cbranch_vccnz .LBB0_345
	s_lshl_b32 s4, s67, 10
	s_lshl_b32 s5, s95, 8
	s_or_b32 s16, s4, s5
	s_and_b64 s[4:5], s[44:45], exec
	s_cselect_b32 s4, 8, 0
	v_lshlrev_b32_e32 v128, 3, v156
	s_or_b32 s4, s4, s16
	v_and_b32_e32 v128, 0xf0, v128
	v_or_b32_e32 v128, s4, v128
	v_or_b32_e32 v204, v128, v202
	v_lshlrev_b64 v[128:129], 12, v[204:205]
	v_lshl_add_u64 v[128:129], s[6:7], 0, v[128:129]
	s_lshl_b32 s36, s36, 7
	v_lshl_add_u64 v[128:129], v[128:129], 0, s[36:37]
	v_lshl_add_u64 v[128:129], v[128:129], 0, v[200:201]
	v_add_co_u32_e32 v130, vcc, 0x1000, v128
	global_store_dword v[128:129], v152, off
	s_nop 0
	v_addc_co_u32_e32 v131, vcc, 0, v129, vcc
	global_store_dword v[130:131], v153, off
	v_add_co_u32_e32 v130, vcc, 0x2000, v128
	s_nop 1
	v_addc_co_u32_e32 v131, vcc, 0, v129, vcc
	v_add_co_u32_e32 v128, vcc, 0x3000, v128
	global_store_dword v[130:131], v154, off
	s_nop 0
	v_addc_co_u32_e32 v129, vcc, 0, v129, vcc
	global_store_dword v[128:129], v155, off
	s_branch .LBB0_345
